# ml_kvloc: next-tile k-slice prefetch loads land directly in the registers the next iteration reads; the two vmcnt(0)+copy pairs per key tile removed, one wait at the top of the next iteration; on top
# speedup vs baseline: 1.0161x; 1.0000x over previous
.LBB0_370:
	s_or_b64 exec, exec, s[64:65]
	s_lshl_b32 s40, s62, 7
	v_cmp_gt_u32_e32 vcc, s74, v226
	v_lshlrev_b32_e32 v22, 1, v108
	v_mov_b32_e32 v10, v6
	v_mov_b32_e32 v11, v6
	v_mov_b32_e32 v12, v6
	v_mov_b32_e32 v13, v6
	v_mov_b32_e32 v14, v6
	v_mov_b32_e32 v15, v6
	v_mov_b32_e32 v16, v6
	v_mov_b32_e32 v17, v6
	s_and_saveexec_b64 s[64:65], vcc
	s_cbranch_execz .LBB0_372
	v_add_u32_e32 v4, s75, v226
	v_mov_b64_e32 v[2:3], s[82:83]
	v_mad_i64_i32 v[2:3], s[76:77], v4, s71, v[2:3]
	v_lshl_add_u64 v[2:3], s[40:41], 1, v[2:3]
	v_mov_b32_e32 v23, v6
	v_lshl_add_u64 v[2:3], v[2:3], 0, v[22:23]
	global_load_dwordx4 v[10:13], v[2:3], off offset:1024
.LBB0_372:
	s_or_b64 exec, exec, s[64:65]
	v_cmp_gt_u32_e32 vcc, s74, v124
	s_and_saveexec_b64 s[64:65], vcc
	s_cbranch_execz .LBB0_374
	v_add_u32_e32 v7, s75, v124
	v_mov_b64_e32 v[8:9], s[82:83]
	v_mad_i64_i32 v[8:9], s[76:77], v7, s71, v[8:9]
	v_lshl_add_u64 v[8:9], s[40:41], 1, v[8:9]
	v_mov_b32_e32 v23, v6
	v_lshl_add_u64 v[8:9], v[8:9], 0, v[22:23]
	global_load_dwordx4 v[14:17], v[8:9], off offset:1024

.LBB0_382:
	s_or_b64 exec, exec, s[64:65]
	s_waitcnt vmcnt(0)
	v_cndmask_b32_e64 v7, 0, v35, s[10:11]
	ds_bpermute_b32 v8, v1, v7
	s_waitcnt lgkmcnt(0)
	s_barrier
	v_add_f32_e32 v8, v7, v8
	v_cndmask_b32_e64 v7, v8, v7, s[12:13]
	ds_bpermute_b32 v8, v107, v7
	s_waitcnt lgkmcnt(0)
	v_add_f32_e32 v8, v7, v8
	v_cndmask_b32_e64 v7, v8, v7, s[14:15]
	ds_bpermute_b32 v8, v109, v7
	s_waitcnt lgkmcnt(0)
	v_add_f32_e32 v8, v7, v8
	v_cndmask_b32_e64 v7, v8, v7, s[16:17]
	ds_bpermute_b32 v8, v111, v7
	s_waitcnt lgkmcnt(0)
	v_add_f32_e32 v8, v7, v8
	v_cndmask_b32_e64 v7, v8, v7, s[18:19]
	ds_bpermute_b32 v8, v120, v7
	s_waitcnt lgkmcnt(0)
	v_add_f32_e32 v8, v7, v8
	v_cndmask_b32_e64 v7, v8, v7, s[4:5]
	ds_bpermute_b32 v8, v121, v7
	s_waitcnt lgkmcnt(0)
	v_add_f32_e32 v8, v7, v8
	s_and_saveexec_b64 s[64:65], s[6:7]
	s_xor_b64 s[64:65], exec, s[64:65]
	v_mov_b32_e32 v9, s68
	ds_write_b32 v9, v8 offset:1024
	s_or_b64 exec, exec, s[64:65]
	v_mov_b32_e32 v9, 0
	s_andn2_b64 vcc, exec, s[42:43]
	v_mov_b32_e32 v35, 0
	s_waitcnt lgkmcnt(0)
	s_barrier
	s_cbranch_vccnz .LBB0_392
	ds_read_b32 v35, v6 offset:1024
	s_waitcnt lgkmcnt(0)
	v_add_f32_e32 v35, 0, v35
	s_andn2_b64 vcc, exec, s[44:45]
	s_cbranch_vccz .LBB0_393

.LBB0_409:
	s_waitcnt vmcnt(0) lgkmcnt(0)
	s_barrier
	ds_read_b32 v8, v167
	v_lshlrev_b32_e32 v103, 16, v11
	v_lshlrev_b32_e32 v102, 16, v10
	v_and_b32_e32 v105, 0xffff0000, v11
	v_and_b32_e32 v104, 0xffff0000, v10
	v_lshlrev_b32_e32 v171, 16, v13
	v_lshlrev_b32_e32 v170, 16, v12
	v_and_b32_e32 v173, 0xffff0000, v13
	v_and_b32_e32 v172, 0xffff0000, v12
	s_waitcnt lgkmcnt(0)
	v_pk_mul_f32 v[102:103], v[8:9], v[102:103] op_sel_hi:[0,1]
	v_pk_mul_f32 v[104:105], v[8:9], v[104:105] op_sel_hi:[0,1]
	v_pk_mul_f32 v[170:171], v[8:9], v[170:171] op_sel_hi:[0,1]
	v_pk_mul_f32 v[8:9], v[8:9], v[172:173] op_sel_hi:[0,1]
	v_bfe_u32 v7, v9, 16, 1
	v_bfe_u32 v169, v8, 16, 1
	v_bfe_u32 v172, v105, 16, 1
	v_bfe_u32 v173, v104, 16, 1
	v_add3_u32 v173, v104, v173, s73
	v_add3_u32 v172, v105, v172, s73
	v_add3_u32 v8, v8, v169, s73
	v_add3_u32 v7, v9, v7, s73
	v_bfe_u32 v9, v102, 16, 1
	v_bfe_u32 v104, v103, 16, 1
	v_bfe_u32 v105, v170, 16, 1
	v_bfe_u32 v169, v171, 16, 1
	v_add3_u32 v169, v171, v169, s73
	v_add3_u32 v105, v170, v105, s73
	v_add3_u32 v103, v103, v104, s73
	v_add3_u32 v9, v102, v9, s73
	v_lshrrev_b32_e32 v9, 16, v9
	v_lshrrev_b32_e32 v102, 16, v103
	v_lshrrev_b32_e32 v103, 16, v105
	v_lshrrev_b32_e32 v104, 16, v169
	v_and_or_b32 v105, v7, s72, v104
	v_and_or_b32 v104, v8, s72, v103
	v_and_or_b32 v103, v172, s72, v102
	v_and_or_b32 v102, v173, s72, v9
	ds_write_b128 v135, v[102:105] offset:2048
	ds_read_b32 v8, v168
	v_lshlrev_b32_e32 v103, 16, v15
	v_lshlrev_b32_e32 v102, 16, v14
	v_and_b32_e32 v105, 0xffff0000, v15
	v_and_b32_e32 v104, 0xffff0000, v14
	v_lshlrev_b32_e32 v171, 16, v17
	v_lshlrev_b32_e32 v170, 16, v16
	v_and_b32_e32 v173, 0xffff0000, v17
	v_and_b32_e32 v172, 0xffff0000, v16
	s_waitcnt lgkmcnt(0)
	v_pk_mul_f32 v[102:103], v[8:9], v[102:103] op_sel_hi:[0,1]
	v_pk_mul_f32 v[104:105], v[8:9], v[104:105] op_sel_hi:[0,1]
	v_pk_mul_f32 v[170:171], v[8:9], v[170:171] op_sel_hi:[0,1]
	v_pk_mul_f32 v[8:9], v[8:9], v[172:173] op_sel_hi:[0,1]
	v_bfe_u32 v7, v9, 16, 1
	v_bfe_u32 v169, v8, 16, 1
	v_bfe_u32 v172, v105, 16, 1
	v_bfe_u32 v173, v104, 16, 1
	v_add3_u32 v173, v104, v173, s73
	v_add3_u32 v172, v105, v172, s73
	v_add3_u32 v8, v8, v169, s73
	v_add3_u32 v7, v9, v7, s73
	v_bfe_u32 v9, v102, 16, 1
	v_bfe_u32 v104, v103, 16, 1
	v_bfe_u32 v105, v170, 16, 1
	v_bfe_u32 v169, v171, 16, 1
	v_add3_u32 v169, v171, v169, s73
	v_add3_u32 v105, v170, v105, s73
	v_add3_u32 v103, v103, v104, s73
	v_add3_u32 v9, v102, v9, s73
	v_lshrrev_b32_e32 v9, 16, v9
	v_lshrrev_b32_e32 v102, 16, v103
	v_lshrrev_b32_e32 v103, 16, v105
	v_lshrrev_b32_e32 v104, 16, v169
	v_and_or_b32 v105, v7, s72, v104
	v_and_or_b32 v104, v8, s72, v103
	v_and_or_b32 v103, v172, s72, v102
	v_and_or_b32 v102, v173, s72, v9
	ds_write_b128 v136, v[102:105] offset:2048
	s_waitcnt vmcnt(0)
	ds_write_b128 v137, v[22:25] offset:19456
	ds_write_b128 v138, v[2:5] offset:19456
	ds_write_b128 v137, v[30:33] offset:37376
	ds_write_b128 v139, v[26:29] offset:19456
	s_and_saveexec_b64 s[26:27], s[22:23]
	ds_write_b128 v140, v[18:21] offset:19968
	s_or_b64 exec, exec, s[26:27]
	s_cmp_ge_u32 s64, s61
	s_cbranch_scc1 .LBB0_408
	v_add_u32_e32 v2, s62, v132
	v_cmp_gt_u32_e32 vcc, s74, v2
	v_mov_b32_e32 v10, v6
	v_mov_b32_e32 v11, v6
	v_mov_b32_e32 v12, v6
	v_mov_b32_e32 v13, v6
	v_mov_b32_e32 v14, v6
	v_mov_b32_e32 v15, v6
	v_mov_b32_e32 v16, v6
	v_mov_b32_e32 v17, v6
	s_and_saveexec_b64 s[26:27], vcc
	s_cbranch_execz .LBB0_414
	v_add_u32_e32 v2, s62, v166
	v_mad_i64_i32 v[2:3], s[76:77], v2, s71, v[116:117]
	global_load_dwordx4 v[10:13], v[2:3], off offset:1024
.LBB0_414:
	s_or_b64 exec, exec, s[26:27]
	v_add_u32_e32 v7, s62, v131
	v_cmp_gt_u32_e32 vcc, s74, v7
	s_and_saveexec_b64 s[26:27], vcc
	s_cbranch_execz .LBB0_416
	v_add_u32_e32 v8, s62, v165
	v_mad_i64_i32 v[8:9], s[76:77], v8, s71, v[116:117]
	global_load_dwordx4 v[14:17], v[8:9], off offset:1024
